# P19/P12: bucket_tab[t] kept in a phase-persistent VGPR (loaded once per phase) so the per-unit T5 LUT setup has one dependent load instead of two
# baseline (speedup 1.0000x reference)
; #define LAS __attribute__((address_space(3)))
; __device__ __forceinline__ int lane_id_v() { int l; asm volatile("v_mbcnt_lo_u32_b32 %0, -1, 0\n\tv_mbcnt_hi_u32_b32 %0, -1, %0" : "=v"(l)); return l & 63; }
; template <int PH>
; __device__ __forceinline__ void mk_body(const Args& a) {
;     ...
;     if (IN(19)) {
;         att::QPre qp{nullptr, 0u, false};
;         for (;;) {
;             const int u = att::next_unit_pre(qp, ctl + CW_Q + 1 * 512, 256, lds, att::OFF_MISC, wave);
;             if (u < 0) break;
;             const int b = u >> 8, h = (u >> 5) & 7, qb = 31 - (u & 31);
;             { const int t_ = wave * 64 + lane_id_v();
;               if (t_ <= 128) ((LAS float*)(lds + att::OFF_LUT))[t_] = (t_ < 128) ? (t5[bucket_tab[t_] * 8 + h] - t5[31 * 8 + h]) * att::LOG2E : 0.f;
;               if (t_ >= 192 && t_ < 256) { const int e_ = (t_ - 192) >> 2, c_ = t_ & 3; ((LAS float*)(lds + att::OFF_LUT + 768))[t_ - 192] = ((e_ >> c_) & 1) ? 0.f : -INFINITY; } }
;             att::Tens T{};
;             T.Q = y0 + Y0_DQ + h * 64; T.ldq = Y0P; T.K = y0 + Y0_DK + h * 64; T.ldk = Y0P; T.V = y0 + Y0_DV + h * 64; T.ldv = Y0P;
;             T.mask = maskg; T.scale2 = 0.125f * att::LOG2E;
.LBB0_1592:
	v_readlane_b32 s2, v254, 0
	v_readlane_b32 s3, v254, 1
	s_cmp_lt_i32 s2, 20
	s_cselect_b64 s[0:1], -1, 0
	s_cmp_gt_i32 s3, 19
	s_cselect_b64 s[2:3], -1, 0
	s_and_b64 s[0:1], s[0:1], s[2:3]
	s_andn2_b64 vcc, exec, s[0:1]
	s_waitcnt lgkmcnt(0)
	s_barrier
	s_cbranch_vccnz .LBB0_1706
	s_add_u32 s6, s54, 0x8800
	s_addc_u32 s7, s55, 0
	s_add_u32 s86, s54, 0x3900000
	s_addc_u32 s87, s55, 0
	s_cmpk_eq_i32 s90, 0xc0
	s_cselect_b64 s[0:1], -1, 0
	s_add_u32 s92, s54, 0x18800c00
	s_addc_u32 s40, s55, 0
	s_add_u32 s41, s54, 0x18801000
	s_addc_u32 s44, s55, 0
	v_writelane_b32 v254, s0, 57
	s_add_u32 s45, s54, 0x18801400
	s_addc_u32 s46, s55, 0
	v_writelane_b32 v254, s1, 58
	s_add_u32 s47, s54, 0x14800000
	v_readlane_b32 s0, v254, 24
	s_addc_u32 s48, s55, 0
	s_lshl_b32 s65, s0, 8
	s_lshl_b32 s49, s0, 5
	s_add_i32 s72, s65, 0
	s_lshl_b32 s64, s0, 3
	s_lshl_b32 s66, s0, 10
	s_mov_b32 s13, 0
	s_add_i32 s67, s72, 0x18000
	s_add_i32 s68, s72, 0x18800
	s_add_i32 s69, s72, 0x19000
	s_add_i32 s70, s72, 0x19800
	s_add_i32 s71, s72, 0x1a000
	s_add_i32 s72, s72, 0x1a800
	s_add_i32 s73, s49, 0xffffff80
	v_mov_b32_e32 v66, 0
	v_mov_b32_e32 v103, 0
	s_movk_i32 s74, 0x100
	v_mov_b32_e32 v88, 1
	s_mov_b32 s14, 0x3e38aa3b
	s_movk_i32 s76, 0x7fff
	s_mov_b32 s78, 0x7060302
	s_add_i32 s79, 0, 0x1fb00
	s_mov_b32 s80, 0x47800000
	v_mov_b32_e32 v89, 0xff800000
	v_mov_b32_e32 v90, 0x4280
	v_mov_b32_e32 v91, 0x3f80
	v_mov_b32_e32 v92, 0x3f803f80
	v_mov_b32_e32 v93, 0x80
	v_mov_b32_e32 v94, 0
	v_mbcnt_lo_u32_b32 v253, -1, 0
	v_mbcnt_hi_u32_b32 v253, -1, v253
	v_and_or_b32 v253, v253, 63, s90
	v_min_u32_e32 v253, 0x7f, v253
	v_lshlrev_b32_e32 v253, 2, v253
	global_load_dword v253, v253, s[86:87]
	s_waitcnt vmcnt(0)
	s_branch .LBB0_1595

; #define LAS __attribute__((address_space(3)))
; __device__ __forceinline__ int lane_id_v() { int l; asm volatile("v_mbcnt_lo_u32_b32 %0, -1, 0\n\tv_mbcnt_hi_u32_b32 %0, -1, %0" : "=v"(l)); return l & 63; }
; template <int PH>
; __device__ __forceinline__ void mk_body(const Args& a) {
;     ...
;             const int u = att::next_unit_pre(qp, ctl + CW_Q + 1 * 512, 256, lds, att::OFF_MISC, wave);
;             if (u < 0) break;
;             const int b = u >> 8, h = (u >> 5) & 7, qb = 31 - (u & 31);
;             { const int t_ = wave * 64 + lane_id_v();
;               if (t_ <= 128) ((LAS float*)(lds + att::OFF_LUT))[t_] = (t_ < 128) ? (t5[bucket_tab[t_] * 8 + h] - t5[31 * 8 + h]) * att::LOG2E : 0.f;
;               if (t_ >= 192 && t_ < 256) { const int e_ = (t_ - 192) >> 2, c_ = t_ & 3; ((LAS float*)(lds + att::OFF_LUT + 768))[t_ - 192] = ((e_ >> c_) & 1) ? 0.f : -INFINITY; } }
.LBB0_1611:
	v_add_u32_e32 v0, 0, v0
	s_waitcnt lgkmcnt(0)
	s_barrier
	ds_read_b32 v0, v0
	s_waitcnt lgkmcnt(0)
	s_barrier
	v_readfirstlane_b32 s8, v0
	s_cmp_lt_i32 s8, 0
	s_cbranch_scc1 .LBB0_1705
	v_mbcnt_lo_u32_b32 v2, -1, 0
	v_mbcnt_hi_u32_b32 v2, -1, v2
	s_movk_i32 s2, 0x81
	v_and_or_b32 v0, v2, 63, s90
	s_bfe_u32 s1, s8, 0x30005
	v_cmp_gt_i32_e32 vcc, s2, v0
	s_and_saveexec_b64 s[2:3], vcc
	s_cbranch_execz .LBB0_1616
	s_movk_i32 s4, 0x80
	v_cmp_ne_u32_e32 vcc, s4, v0
	v_mov_b32_e32 v1, 0
	s_and_saveexec_b64 s[4:5], vcc
	s_cbranch_execz .LBB0_1615
	v_mov_b32_e32 v1, v253
	s_lshl_b32 s9, s1, 2
	v_mov_b32_e32 v3, s9
	v_lshl_or_b32 v4, v1, 3, s1
	v_ashrrev_i32_e32 v5, 31, v4
	v_lshl_add_u64 v[4:5], v[4:5], 2, s[42:43]
	global_load_dword v1, v[4:5], off
	s_nop 0
	global_load_dword v3, v3, s[42:43] offset:992
	s_waitcnt vmcnt(0)
	v_sub_f32_e32 v1, v1, v3
	v_mul_f32_e32 v1, 0x3fb8aa3b, v1

; #define LAS __attribute__((address_space(3)))
; __device__ __forceinline__ int lane_id_v() { int l; asm volatile("v_mbcnt_lo_u32_b32 %0, -1, 0\n\tv_mbcnt_hi_u32_b32 %0, -1, %0" : "=v"(l)); return l & 63; }
; template <int PH>
; __device__ __forceinline__ void mk_body(const Args& a) {
;     ...
;         {
;             float s1 = 0.f, s2 = 0.f;
;             for (int i = 0; i < 64; ++i) { s1 += a.in[7][i] * a.in[8][i]; s2 += a.in[9][i] * a.in[10][i]; }
;             lam = expf(s1) - expf(s2) + LAMBDA_INIT;
;         }
;         for (;;) {
;             const int u = att::next_unit_pre(qp, ctl + CW_Q + 2 * 512, 128, lds, att::OFF_MISC, wave);
;             if (u < 0) break;
;             const int b = u >> 7, h = (u >> 5) & 3, qb = 31 - (u & 31);
;             att::f32x16 oa[4];
; #pragma unroll 1
;             for (int mp = 0; mp < 2; ++mp) {
;                 const int mh = 2 * h + mp;
;                 { const int t_ = wave * 64 + lane_id_v(); if (t_ <= 128) ((LAS float*)(lds + att::OFF_LUT))[t_] = (t_ < 128) ? (t5[bucket_tab[t_] * 8 + mh] - t5[31 * 8 + mh]) * att::LOG2E : 0.f; }
.LBB0_2369:
	s_add_u32 s0, s66, s2
	s_addc_u32 s1, s67, s3
	global_load_dwordx4 v[4:7], v2, s[0:1]
	global_load_dwordx4 v[8:11], v2, s[0:1] offset:16
	s_add_u32 s0, s56, s2
	s_addc_u32 s1, s57, s3
	global_load_dwordx4 v[12:15], v2, s[0:1]
	global_load_dwordx4 v[16:19], v2, s[0:1] offset:16
	s_add_u32 s0, s58, s2
	s_addc_u32 s1, s59, s3
	global_load_dwordx4 v[20:23], v2, s[0:1]
	global_load_dwordx4 v[24:27], v2, s[0:1] offset:16
	s_add_u32 s0, s60, s2
	s_addc_u32 s1, s61, s3
	global_load_dwordx4 v[28:31], v2, s[0:1]
	global_load_dwordx4 v[32:35], v2, s[0:1] offset:16
	s_add_u32 s2, s2, 32
	s_addc_u32 s3, s3, 0
	s_cmpk_eq_i32 s2, 0x100
	s_waitcnt vmcnt(0)
	v_mov_b32_e32 v36, v4
	v_mov_b32_e32 v4, v6
	v_mov_b32_e32 v6, v8
	v_mov_b32_e32 v8, v10
	v_mov_b32_e32 v10, v12
	v_mov_b32_e32 v12, v14
	v_mov_b32_e32 v37, v20
	v_mov_b32_e32 v20, v5
	v_mov_b32_e32 v5, v22
	v_mov_b32_e32 v22, v7
	v_mov_b32_e32 v7, v24
	v_mov_b32_e32 v24, v9
	v_mov_b32_e32 v9, v26
	v_mov_b32_e32 v26, v11
	v_mov_b32_e32 v11, v28
	v_mov_b32_e32 v28, v13
	v_pk_fma_f32 v[0:1], v[36:37], v[10:11], v[0:1]
	v_mov_b32_e32 v13, v30
	v_pk_fma_f32 v[0:1], v[20:21], v[28:29], v[0:1]
	v_mov_b32_e32 v30, v15
	v_pk_fma_f32 v[0:1], v[4:5], v[12:13], v[0:1]
	v_mov_b32_e32 v14, v16
	v_mov_b32_e32 v15, v32
	v_pk_fma_f32 v[0:1], v[22:23], v[30:31], v[0:1]
	v_mov_b32_e32 v32, v17
	v_pk_fma_f32 v[0:1], v[6:7], v[14:15], v[0:1]
	v_mov_b32_e32 v16, v18
	v_mov_b32_e32 v17, v34
	v_pk_fma_f32 v[0:1], v[24:25], v[32:33], v[0:1]
	v_mov_b32_e32 v34, v19
	v_pk_fma_f32 v[0:1], v[8:9], v[16:17], v[0:1]
	s_nop 0
	v_pk_fma_f32 v[0:1], v[26:27], v[34:35], v[0:1]
	s_cbranch_scc0 .LBB0_2369
	v_mul_f32_e32 v2, 0x3fb8aa3b, v0
	s_mov_b32 s0, 0x3fb8aa3b
	v_rndne_f32_e32 v3, v2
	v_sub_f32_e32 v4, v2, v3
	v_fma_f32 v2, v0, s0, -v2
	v_fmac_f32_e32 v2, 0x32a5705f, v0
	v_add_f32_e32 v2, v4, v2
	v_exp_f32_e32 v2, v2
	v_cvt_i32_f32_e32 v3, v3
	s_mov_b32 s1, 0xc2ce8ed0
	v_cmp_ngt_f32_e32 vcc, s1, v0
	s_mov_b32 s2, 0x42b17218
	v_ldexp_f32 v2, v2, v3
	v_mul_f32_e32 v3, 0x3fb8aa3b, v1
	v_rndne_f32_e32 v4, v3
	v_sub_f32_e32 v5, v3, v4
	v_fma_f32 v3, v1, s0, -v3
	v_fmac_f32_e32 v3, 0x32a5705f, v1
	v_cndmask_b32_e32 v2, 0, v2, vcc
	v_add_f32_e32 v3, v5, v3
	v_mov_b32_e32 v5, 0x7f800000
	v_cmp_nlt_f32_e32 vcc, s2, v0
	s_add_u32 s0, s54, 0x9000
	v_exp_f32_e32 v3, v3
	v_cndmask_b32_e32 v0, v5, v2, vcc
	v_cmp_ngt_f32_e32 vcc, s1, v1
	s_addc_u32 s1, s55, 0
	s_add_u32 s38, s54, 0x3900000
	s_addc_u32 s39, s55, 0
	s_add_u32 s45, s54, 0x18800000
	v_writelane_b32 v254, s0, 31
	s_addc_u32 s74, s55, 0
	v_cvt_i32_f32_e32 v4, v4
	v_writelane_b32 v254, s1, 32
	s_add_u32 s0, s54, 0x18800400
	v_writelane_b32 v254, s0, 8
	s_addc_u32 s0, s55, 0
	v_writelane_b32 v254, s0, 57
	s_add_u32 s0, s54, 0x18800800
	v_writelane_b32 v254, s0, 59
	s_addc_u32 s0, s55, 0
	v_ldexp_f32 v2, v3, v4
	v_writelane_b32 v254, s0, 30
	v_cndmask_b32_e32 v2, 0, v2, vcc
	v_cmp_nlt_f32_e32 vcc, s2, v1
	v_readlane_b32 s0, v254, 24
	s_lshl_b32 s79, s0, 5
	v_cndmask_b32_e32 v1, v5, v2, vcc
	s_lshl_b32 s80, s0, 3
	s_lshl_b32 s81, s0, 10
	s_lshl_b32 s82, s0, 11
	v_sub_f32_e32 v0, v0, v1
	s_add_u32 s40, s54, 0xc800000
	v_mbcnt_lo_u32_b32 v1, -1, 0
	s_mov_b32 s35, 0
	v_add_f32_e32 v146, 0x3eb60549, v0
	s_addc_u32 s41, s55, 0
	v_mov_b32_e32 v145, 0
	s_movk_i32 s84, 0x80
	s_mov_b32 s44, 0x3e38aa3b
	s_movk_i32 s85, 0x7fff
	s_mov_b32 s86, 0x7060302
	s_mov_b32 s87, 0x8000
	s_mov_b32 s88, 0x47800000
	v_mov_b32_e32 v147, 0x358637bd
	v_mov_b32_e32 v148, 0x260
	v_mov_b32_e32 v0, 0x42800000
	v_mov_b32_e32 v149, 0x80
	v_mov_b32_e32 v150, 0xff800000
	v_mbcnt_hi_u32_b32 v151, -1, v1
	v_mbcnt_lo_u32_b32 v253, -1, 0
	v_mbcnt_hi_u32_b32 v253, -1, v253
	v_and_or_b32 v253, v253, 63, s90
	v_min_u32_e32 v253, 0x7f, v253
	v_lshlrev_b32_e32 v253, 2, v253
	global_load_dword v253, v253, s[38:39]
	s_waitcnt vmcnt(0)
	s_branch .LBB0_2372

; #define LAS __attribute__((address_space(3)))
; __device__ __forceinline__ int lane_id_v() { int l; asm volatile("v_mbcnt_lo_u32_b32 %0, -1, 0\n\tv_mbcnt_hi_u32_b32 %0, -1, %0" : "=v"(l)); return l & 63; }
; template <int PH>
; __device__ __forceinline__ void mk_body(const Args& a) {
;     ...
;                 { const int t_ = wave * 64 + lane_id_v(); if (t_ <= 128) ((LAS float*)(lds + att::OFF_LUT))[t_] = (t_ < 128) ? (t5[bucket_tab[t_] * 8 + mh] - t5[31 * 8 + mh]) * att::LOG2E : 0.f; }
.LBB0_2434:
	s_or_b32 s34, s0, s94
	v_mbcnt_lo_u32_b32 v1, -1, 0
	v_mbcnt_hi_u32_b32 v1, -1, v1
	s_movk_i32 s0, 0x81
	v_and_or_b32 v2, v1, 63, s90
	v_cmp_gt_i32_e32 vcc, s0, v2
	s_and_saveexec_b64 s[4:5], vcc
	s_cbranch_execz .LBB0_2438
	v_cmp_ne_u32_e32 vcc, s84, v2
	v_mov_b32_e32 v1, 0
	s_and_saveexec_b64 s[6:7], vcc
	s_cbranch_execz .LBB0_2437
	v_mov_b32_e32 v1, v253
	s_lshl_b64 s[0:1], s[34:35], 2
	s_add_u32 s0, s42, s0
	s_addc_u32 s1, s43, s1
	v_lshl_or_b32 v4, v1, 3, s34
	v_ashrrev_i32_e32 v5, 31, v4
	v_lshl_add_u64 v[4:5], v[4:5], 2, s[42:43]
	global_load_dword v1, v[4:5], off
	global_load_dword v3, v145, s[0:1] offset:992
	s_waitcnt vmcnt(0)
	v_sub_f32_e32 v1, v1, v3
	v_mul_f32_e32 v1, 0x3fb8aa3b, v1
